# phase 4 gated conv loop: the 12 loads of a 4-token group issued together into staging registers (was 3 loads then a full wait per token); on top of v44
# speedup vs baseline: 1.0057x; 1.0057x over previous
; #define GAS __attribute__((address_space(1)))
; __device__ __forceinline__ u32x2 pack4(f32x4 v) { u32x2 w; w.x = pk2(v.x, v.y); w.y = pk2(v.z, v.w); return w; }
; __device__ __forceinline__ f32x4 unpack4(u32x2 w) { return (f32x4){bflo(w.x), bfhi(w.x), bflo(w.y), bfhi(w.y)}; }
; __device__ __forceinline__ void phase4(KP kp, int wave, int bid, int G) {
;     ...
;         for (int i = 0; i < 16; ++i) { const int t = t0 + i; const bf16* r = R + (size_t)t * 10240 + ch;
;             const v4u b = *(const GAS v4u*)r, c = *(const GAS v4u*)(r + 2048), h = *(const GAS v4u*)(r + 4096);
;             const f32x4 ua = unpack4((u32x2){c.x, c.y}) * unpack4((u32x2){h.x, h.y}), ub = unpack4((u32x2){c.z, c.w}) * unpack4((u32x2){h.z, h.w});
;             const f32x4 ya = unpack4((u32x2){b.x, b.y}) * (w0a * u2a + w1a * u1a + w2a * ua), yb = unpack4((u32x2){b.z, b.w}) * (w0b * u2b + w1b * u1b + w2b * ub);
;             const u32x2 pa = pack4(ya), pb = pack4(yb);
;             *(GAS v4u*)(CV + (size_t)t * 4096 + ch) = (v4u){pa.x, pa.y, pb.x, pb.y};
;             u2a = u1a; u2b = u1b; u1a = ua; u1b = ub; }
.LBB0_715:
	s_waitcnt vmcnt(4)
	v_pk_mul_f32 v[32:33], v[8:9], v[32:33]
	v_lshl_add_u64 v[2:3], s[14:15], 0, v[46:47]
	v_pk_mul_f32 v[60:61], v[8:9], v[36:37]
	s_waitcnt vmcnt(2)
	v_pk_fma_f32 v[68:69], v[16:17], v[36:37], v[32:33]
	v_add_co_u32_e64 v36, s[2:3], s29, v2
	v_lshl_add_u64 v[48:49], s[26:27], 0, v[46:47]
	v_pk_mul_f32 v[34:35], v[10:11], v[34:35]
	v_addc_co_u32_e64 v37, s[2:3], 0, v3, s[2:3]
	v_pk_fma_f32 v[66:67], v[18:19], v[38:39], v[34:35]
	v_add_co_u32_e64 v34, s[2:3], s30, v48
	v_pk_mul_f32 v[28:29], v[4:5], v[28:29]
	s_nop 0
	v_addc_co_u32_e64 v35, s[2:3], 0, v49, s[2:3]
	v_add_co_u32_e64 v72, s[2:3], s31, v48
	v_pk_fma_f32 v[70:71], v[12:13], v[40:41], v[28:29]
	s_nop 0
	v_addc_co_u32_e64 v73, s[2:3], 0, v49, s[2:3]
	v_add_co_u32_e64 v28, s[2:3], s34, v2
	v_pk_mul_f32 v[30:31], v[6:7], v[30:31]
	s_nop 0
	v_addc_co_u32_e64 v29, s[2:3], 0, v3, s[2:3]
	v_pk_mul_f32 v[62:63], v[6:7], v[42:43]
	v_pk_fma_f32 v[42:43], v[14:15], v[42:43], v[30:31]
	v_add_co_u32_e64 v30, s[2:3], s35, v48
	v_add_co_u32_e32 v50, vcc, 0x3e000000, v48
	s_nop 0
	v_addc_co_u32_e64 v31, s[2:3], 0, v49, s[2:3]
	v_add_co_u32_e64 v32, s[2:3], s36, v48
	v_addc_co_u32_e32 v51, vcc, 0, v49, vcc
	s_nop 0
	v_addc_co_u32_e64 v33, s[2:3], 0, v49, s[2:3]
	v_add_co_u32_e64 v74, s[2:3], s37, v2
	v_add_co_u32_e32 v52, vcc, 0x3e001000, v48
	s_nop 0
	v_addc_co_u32_e64 v75, s[2:3], 0, v3, s[2:3]
	v_add_co_u32_e64 v76, s[2:3], s38, v48
	v_addc_co_u32_e32 v53, vcc, 0, v49, vcc
	s_nop 0
	v_addc_co_u32_e64 v77, s[2:3], 0, v49, s[2:3]
	v_add_co_u32_e64 v78, s[2:3], s39, v48
	v_add_co_u32_e32 v48, vcc, 0x3e002000, v48
	s_nop 0
	v_addc_co_u32_e64 v79, s[2:3], 0, v49, s[2:3]
	v_addc_co_u32_e32 v49, vcc, 0, v49, vcc
	v_pk_mul_f32 v[58:59], v[10:11], v[38:39]
	v_pk_mul_f32 v[64:65], v[4:5], v[40:41]
	global_load_dwordx4 v[160:163], v[50:51], off
	global_load_dwordx4 v[164:167], v[48:49], off
	global_load_dwordx4 v[168:171], v[52:53], off
	global_load_dwordx4 v[172:175], v[34:35], off
	global_load_dwordx4 v[176:179], v[72:73], off
	global_load_dwordx4 v[180:183], v[34:35], off offset:-4096
	global_load_dwordx4 v[184:187], v[30:31], off
	global_load_dwordx4 v[188:191], v[32:33], off
	global_load_dwordx4 v[192:195], v[30:31], off offset:-4096
	global_load_dwordx4 v[196:199], v[76:77], off
	global_load_dwordx4 v[200:203], v[78:79], off
	global_load_dwordx4 v[204:207], v[76:77], off offset:-4096
	s_add_u32 s14, s14, 0x8000
	s_addc_u32 s15, s15, 0
	s_add_u32 s26, s26, 0x14000
	s_addc_u32 s27, s27, 0
	s_add_i32 s41, s41, -4
	v_add_co_u32_e32 v2, vcc, s40, v2
	s_cmp_eq_u32 s41, 0
	s_nop 0
	v_addc_co_u32_e32 v3, vcc, 0, v3, vcc
	s_waitcnt vmcnt(9)
	v_mov_b32_e32 v38, v160
	v_mov_b32_e32 v39, v161
	v_mov_b32_e32 v40, v162
	v_mov_b32_e32 v41, v163
	v_mov_b32_e32 v54, v164
	v_mov_b32_e32 v55, v165
	v_mov_b32_e32 v56, v166
	v_mov_b32_e32 v57, v167
	v_mov_b32_e32 v50, v168
	v_mov_b32_e32 v51, v169
	v_mov_b32_e32 v52, v170
	v_mov_b32_e32 v53, v171
	v_lshlrev_b32_e32 v48, 16, v38
	v_lshlrev_b32_e32 v86, 16, v54
	v_and_b32_e32 v87, 0xffff0000, v54
	v_lshlrev_b32_e32 v82, 16, v50
	v_and_b32_e32 v83, 0xffff0000, v50
	v_lshlrev_b32_e32 v50, 16, v51
	v_and_b32_e32 v51, 0xffff0000, v51
	v_lshlrev_b32_e32 v84, 16, v52
	v_and_b32_e32 v85, 0xffff0000, v52
	v_lshlrev_b32_e32 v52, 16, v53
	v_and_b32_e32 v53, 0xffff0000, v53
	v_lshlrev_b32_e32 v54, 16, v55
	v_and_b32_e32 v55, 0xffff0000, v55
	v_lshlrev_b32_e32 v88, 16, v56
	v_and_b32_e32 v89, 0xffff0000, v56
	v_lshlrev_b32_e32 v56, 16, v57
	v_and_b32_e32 v57, 0xffff0000, v57
	v_pk_mul_f32 v[50:51], v[50:51], v[54:55]
	v_pk_mul_f32 v[54:55], v[82:83], v[86:87]
	v_pk_mul_f32 v[52:53], v[52:53], v[56:57]
	v_pk_mul_f32 v[56:57], v[84:85], v[88:89]
	v_and_b32_e32 v49, 0xffff0000, v38
	v_lshlrev_b32_e32 v38, 16, v39
	v_and_b32_e32 v39, 0xffff0000, v39
	v_lshlrev_b32_e32 v80, 16, v40
	v_and_b32_e32 v81, 0xffff0000, v40
	v_lshlrev_b32_e32 v40, 16, v41
	v_and_b32_e32 v41, 0xffff0000, v41
	v_pk_fma_f32 v[68:69], v[24:25], v[54:55], v[68:69]
	v_pk_fma_f32 v[66:67], v[26:27], v[50:51], v[66:67]
	v_pk_fma_f32 v[70:71], v[20:21], v[56:57], v[70:71]
	v_pk_fma_f32 v[42:43], v[22:23], v[52:53], v[42:43]
	v_pk_mul_f32 v[38:39], v[66:67], v[38:39]
	v_pk_mul_f32 v[48:49], v[68:69], v[48:49]
	v_pk_mul_f32 v[40:41], v[42:43], v[40:41]
	v_pk_mul_f32 v[42:43], v[70:71], v[80:81]
	v_pk_fma_f32 v[58:59], v[18:19], v[50:51], v[58:59]
	v_pk_mul_f32 v[82:83], v[10:11], v[50:51]
	v_bfe_u32 v1, v48, 16, 1
	v_bfe_u32 v50, v38, 16, 1
	v_bfe_u32 v66, v42, 16, 1
	v_bfe_u32 v68, v40, 16, 1
	v_bfe_u32 v45, v49, 16, 1
	v_bfe_u32 v51, v39, 16, 1
	v_bfe_u32 v67, v43, 16, 1
	v_bfe_u32 v69, v41, 16, 1
	v_add3_u32 v1, v48, v1, s28
	v_add3_u32 v38, v38, v50, s28
	v_add3_u32 v42, v42, v66, s28
	v_add3_u32 v40, v40, v68, s28
	v_add3_u32 v45, v49, v45, s28
	v_add3_u32 v39, v39, v51, s28
	v_add3_u32 v43, v43, v67, s28
	v_add3_u32 v41, v41, v69, s28
	v_lshrrev_b32_e32 v1, 16, v1
	v_lshrrev_b32_e32 v48, 16, v38
	v_lshrrev_b32_e32 v42, 16, v42
	v_lshrrev_b32_e32 v49, 16, v40
	v_and_or_b32 v38, v45, s25, v1
	v_and_or_b32 v39, v39, s25, v48
	v_and_or_b32 v40, v43, s25, v42
	v_and_or_b32 v41, v41, s25, v49
	global_store_dwordx4 v[36:37], v[38:41], off
	s_nop 0
	v_pk_fma_f32 v[60:61], v[16:17], v[54:55], v[60:61]
	v_pk_fma_f32 v[62:63], v[14:15], v[52:53], v[62:63]
	v_pk_fma_f32 v[64:65], v[12:13], v[56:57], v[64:65]
	v_pk_mul_f32 v[54:55], v[8:9], v[54:55]
	v_pk_mul_f32 v[56:57], v[4:5], v[56:57]
	v_pk_mul_f32 v[52:53], v[6:7], v[52:53]
	s_waitcnt vmcnt(7)
; #define GAS __attribute__((address_space(1)))
; __device__ __forceinline__ u32x2 pack4(f32x4 v) { u32x2 w; w.x = pk2(v.x, v.y); w.y = pk2(v.z, v.w); return w; }
; __device__ __forceinline__ f32x4 unpack4(u32x2 w) { return (f32x4){bflo(w.x), bfhi(w.x), bflo(w.y), bfhi(w.y)}; }
; __device__ __forceinline__ void phase4(KP kp, int wave, int bid, int G) {
;     ...
;         for (int i = 0; i < 16; ++i) { const int t = t0 + i; const bf16* r = R + (size_t)t * 10240 + ch;
;             const v4u b = *(const GAS v4u*)r, c = *(const GAS v4u*)(r + 2048), h = *(const GAS v4u*)(r + 4096);
;             const f32x4 ua = unpack4((u32x2){c.x, c.y}) * unpack4((u32x2){h.x, h.y}), ub = unpack4((u32x2){c.z, c.w}) * unpack4((u32x2){h.z, h.w});
;             const f32x4 ya = unpack4((u32x2){b.x, b.y}) * (w0a * u2a + w1a * u1a + w2a * ua), yb = unpack4((u32x2){b.z, b.w}) * (w0b * u2b + w1b * u1b + w2b * ub);
;             const u32x2 pa = pack4(ya), pb = pack4(yb);
;             *(GAS v4u*)(CV + (size_t)t * 4096 + ch) = (v4u){pa.x, pa.y, pb.x, pb.y};
;             u2a = u1a; u2b = u1b; u1a = ua; u1b = ub; }
	v_mov_b32_e32 v36, v172
	v_mov_b32_e32 v37, v173
	v_mov_b32_e32 v38, v174
	v_mov_b32_e32 v39, v175
	v_mov_b32_e32 v40, v176
	v_mov_b32_e32 v41, v177
	v_mov_b32_e32 v42, v178
	v_mov_b32_e32 v43, v179
	v_mov_b32_e32 v48, v180
	v_mov_b32_e32 v49, v181
	v_mov_b32_e32 v50, v182
	v_mov_b32_e32 v51, v183
	v_lshlrev_b32_e32 v34, 16, v36
	v_and_b32_e32 v35, 0xffff0000, v36
	v_lshlrev_b32_e32 v36, 16, v37
	v_and_b32_e32 v37, 0xffff0000, v37
	v_lshlrev_b32_e32 v66, 16, v40
	v_and_b32_e32 v67, 0xffff0000, v40
	v_lshlrev_b32_e32 v40, 16, v41
	v_and_b32_e32 v41, 0xffff0000, v41
	v_lshlrev_b32_e32 v68, 16, v38
	v_and_b32_e32 v69, 0xffff0000, v38
	v_lshlrev_b32_e32 v38, 16, v39
	v_and_b32_e32 v39, 0xffff0000, v39
	v_lshlrev_b32_e32 v70, 16, v42
	v_and_b32_e32 v71, 0xffff0000, v42
	v_lshlrev_b32_e32 v42, 16, v43
	v_and_b32_e32 v43, 0xffff0000, v43
	v_pk_mul_f32 v[84:85], v[36:37], v[40:41]
	v_pk_mul_f32 v[66:67], v[34:35], v[66:67]
	v_pk_mul_f32 v[86:87], v[38:39], v[42:43]
	v_pk_mul_f32 v[68:69], v[68:69], v[70:71]
	v_lshlrev_b32_e32 v72, 16, v48
	v_and_b32_e32 v73, 0xffff0000, v48
	v_lshlrev_b32_e32 v48, 16, v49
	v_and_b32_e32 v49, 0xffff0000, v49
	v_lshlrev_b32_e32 v80, 16, v50
	v_and_b32_e32 v81, 0xffff0000, v50
	v_lshlrev_b32_e32 v50, 16, v51
	v_and_b32_e32 v51, 0xffff0000, v51
	v_pk_fma_f32 v[34:35], v[24:25], v[66:67], v[60:61]
	v_pk_fma_f32 v[36:37], v[26:27], v[84:85], v[58:59]
	v_pk_fma_f32 v[38:39], v[20:21], v[68:69], v[64:65]
	v_pk_fma_f32 v[40:41], v[22:23], v[86:87], v[62:63]
	v_pk_mul_f32 v[36:37], v[36:37], v[48:49]
	v_pk_mul_f32 v[34:35], v[34:35], v[72:73]
	v_pk_mul_f32 v[40:41], v[40:41], v[50:51]
	v_pk_mul_f32 v[38:39], v[38:39], v[80:81]
	v_bfe_u32 v1, v34, 16, 1
	v_bfe_u32 v45, v35, 16, 1
	v_bfe_u32 v48, v36, 16, 1
	v_bfe_u32 v49, v37, 16, 1
	v_bfe_u32 v50, v38, 16, 1
	v_bfe_u32 v51, v39, 16, 1
	v_bfe_u32 v58, v40, 16, 1
	v_bfe_u32 v59, v41, 16, 1
	v_add3_u32 v1, v34, v1, s28
	v_add3_u32 v34, v35, v45, s28
	v_add3_u32 v35, v36, v48, s28
	v_add3_u32 v36, v37, v49, s28
	v_add3_u32 v37, v38, v50, s28
	v_add3_u32 v38, v39, v51, s28
	v_add3_u32 v39, v40, v58, s28
	v_add3_u32 v40, v41, v59, s28
	v_lshrrev_b32_e32 v1, 16, v1
	v_lshrrev_b32_e32 v35, 16, v35
	v_lshrrev_b32_e32 v37, 16, v37
	v_lshrrev_b32_e32 v39, 16, v39
	v_and_or_b32 v34, v34, s25, v1
	v_and_or_b32 v35, v36, s25, v35
	v_and_or_b32 v36, v38, s25, v37
	v_and_or_b32 v37, v40, s25, v39
	global_store_dwordx4 v[28:29], v[34:37], off
	s_nop 0
	s_nop 0
	v_pk_fma_f32 v[42:43], v[18:19], v[84:85], v[82:83]
	v_pk_fma_f32 v[54:55], v[16:17], v[66:67], v[54:55]
	v_pk_fma_f32 v[52:53], v[14:15], v[86:87], v[52:53]
	v_pk_fma_f32 v[56:57], v[12:13], v[68:69], v[56:57]
	s_waitcnt vmcnt(5)
; #define GAS __attribute__((address_space(1)))
; __device__ __forceinline__ u32x2 pack4(f32x4 v) { u32x2 w; w.x = pk2(v.x, v.y); w.y = pk2(v.z, v.w); return w; }
; __device__ __forceinline__ f32x4 unpack4(u32x2 w) { return (f32x4){bflo(w.x), bfhi(w.x), bflo(w.y), bfhi(w.y)}; }
; __device__ __forceinline__ void phase4(KP kp, int wave, int bid, int G) {
;     ...
;         for (int i = 0; i < 16; ++i) { const int t = t0 + i; const bf16* r = R + (size_t)t * 10240 + ch;
;             const v4u b = *(const GAS v4u*)r, c = *(const GAS v4u*)(r + 2048), h = *(const GAS v4u*)(r + 4096);
;             const f32x4 ua = unpack4((u32x2){c.x, c.y}) * unpack4((u32x2){h.x, h.y}), ub = unpack4((u32x2){c.z, c.w}) * unpack4((u32x2){h.z, h.w});
;             const f32x4 ya = unpack4((u32x2){b.x, b.y}) * (w0a * u2a + w1a * u1a + w2a * ua), yb = unpack4((u32x2){b.z, b.w}) * (w0b * u2b + w1b * u1b + w2b * ub);
;             const u32x2 pa = pack4(ya), pb = pack4(yb);
;             *(GAS v4u*)(CV + (size_t)t * 4096 + ch) = (v4u){pa.x, pa.y, pb.x, pb.y};
;             u2a = u1a; u2b = u1b; u1a = ua; u1b = ub; }
;     }
	v_mov_b32_e32 v34, v184
	v_mov_b32_e32 v35, v185
	v_mov_b32_e32 v36, v186
	v_mov_b32_e32 v37, v187
	v_mov_b32_e32 v38, v188
	v_mov_b32_e32 v39, v189
	v_mov_b32_e32 v40, v190
	v_mov_b32_e32 v41, v191
	v_mov_b32_e32 v28, v192
	v_mov_b32_e32 v29, v193
	v_mov_b32_e32 v30, v194
	v_mov_b32_e32 v31, v195
	v_lshlrev_b32_e32 v32, 16, v34
	v_and_b32_e32 v33, 0xffff0000, v34
	v_lshlrev_b32_e32 v34, 16, v35
	v_and_b32_e32 v35, 0xffff0000, v35
	v_lshlrev_b32_e32 v48, 16, v38
	v_and_b32_e32 v49, 0xffff0000, v38
	v_lshlrev_b32_e32 v38, 16, v39
	v_and_b32_e32 v39, 0xffff0000, v39
	v_lshlrev_b32_e32 v50, 16, v36
	v_and_b32_e32 v51, 0xffff0000, v36
	v_lshlrev_b32_e32 v36, 16, v37
	v_and_b32_e32 v37, 0xffff0000, v37
	v_lshlrev_b32_e32 v58, 16, v40
	v_and_b32_e32 v59, 0xffff0000, v40
	v_lshlrev_b32_e32 v40, 16, v41
	v_and_b32_e32 v41, 0xffff0000, v41
	v_lshlrev_b32_e32 v60, 16, v28
	v_and_b32_e32 v61, 0xffff0000, v28
	v_lshlrev_b32_e32 v62, 16, v29
	v_and_b32_e32 v63, 0xffff0000, v29
	v_lshlrev_b32_e32 v64, 16, v30
	v_and_b32_e32 v65, 0xffff0000, v30
	v_lshlrev_b32_e32 v70, 16, v31
	v_and_b32_e32 v71, 0xffff0000, v31
	v_pk_mul_f32 v[34:35], v[34:35], v[38:39]
	v_pk_mul_f32 v[32:33], v[32:33], v[48:49]
	v_pk_mul_f32 v[30:31], v[36:37], v[40:41]
	v_pk_mul_f32 v[28:29], v[50:51], v[58:59]
	v_pk_fma_f32 v[36:37], v[24:25], v[32:33], v[54:55]
	v_pk_fma_f32 v[38:39], v[26:27], v[34:35], v[42:43]
	v_pk_fma_f32 v[40:41], v[20:21], v[28:29], v[56:57]
	v_pk_fma_f32 v[42:43], v[22:23], v[30:31], v[52:53]
	v_pk_mul_f32 v[38:39], v[38:39], v[62:63]
	v_pk_mul_f32 v[36:37], v[36:37], v[60:61]
	v_pk_mul_f32 v[42:43], v[42:43], v[70:71]
	v_pk_mul_f32 v[40:41], v[40:41], v[64:65]
	v_bfe_u32 v1, v36, 16, 1
	v_bfe_u32 v45, v37, 16, 1
	v_bfe_u32 v48, v38, 16, 1
	v_bfe_u32 v49, v39, 16, 1
	v_bfe_u32 v50, v40, 16, 1
	v_bfe_u32 v51, v41, 16, 1
	v_bfe_u32 v52, v42, 16, 1
	v_bfe_u32 v53, v43, 16, 1
	v_add3_u32 v1, v36, v1, s28
	v_add3_u32 v36, v37, v45, s28
	v_add3_u32 v37, v38, v48, s28
	v_add3_u32 v38, v39, v49, s28
	v_add3_u32 v39, v40, v50, s28
	v_add3_u32 v40, v41, v51, s28
	v_add3_u32 v41, v42, v52, s28
	v_add3_u32 v42, v43, v53, s28
	v_lshrrev_b32_e32 v1, 16, v1
	v_lshrrev_b32_e32 v37, 16, v37
	v_lshrrev_b32_e32 v39, 16, v39
	v_lshrrev_b32_e32 v41, 16, v41
	v_and_or_b32 v36, v36, s25, v1
	v_and_or_b32 v37, v38, s25, v37
	v_and_or_b32 v38, v40, s25, v39
	v_and_or_b32 v39, v42, s25, v41
	global_store_dwordx4 v[74:75], v[36:39], off
	s_nop 0
	v_pk_mul_f32 v[52:53], v[8:9], v[66:67]
	v_pk_mul_f32 v[54:55], v[10:11], v[84:85]
	v_pk_mul_f32 v[56:57], v[4:5], v[68:69]
	v_pk_mul_f32 v[58:59], v[6:7], v[86:87]
	v_pk_fma_f32 v[54:55], v[18:19], v[34:35], v[54:55]
	v_pk_fma_f32 v[52:53], v[16:17], v[32:33], v[52:53]
	v_pk_fma_f32 v[58:59], v[14:15], v[30:31], v[58:59]
	v_pk_fma_f32 v[56:57], v[12:13], v[28:29], v[56:57]
	s_waitcnt vmcnt(3)
	v_mov_b32_e32 v36, v196
	v_mov_b32_e32 v37, v197
	v_mov_b32_e32 v38, v198
	v_mov_b32_e32 v39, v199
	v_mov_b32_e32 v40, v200
	v_mov_b32_e32 v41, v201
	v_mov_b32_e32 v42, v202
	v_mov_b32_e32 v43, v203
	v_mov_b32_e32 v48, v204
	v_mov_b32_e32 v49, v205
	v_mov_b32_e32 v50, v206
	v_mov_b32_e32 v51, v207
	v_lshlrev_b32_e32 v60, 16, v36
	v_and_b32_e32 v61, 0xffff0000, v36
	v_lshlrev_b32_e32 v36, 16, v37
	v_and_b32_e32 v37, 0xffff0000, v37
	v_lshlrev_b32_e32 v62, 16, v40
	v_and_b32_e32 v63, 0xffff0000, v40
	v_lshlrev_b32_e32 v40, 16, v41
	v_and_b32_e32 v41, 0xffff0000, v41
	v_lshlrev_b32_e32 v64, 16, v38
	v_and_b32_e32 v65, 0xffff0000, v38
	v_lshlrev_b32_e32 v66, 16, v39
	v_and_b32_e32 v67, 0xffff0000, v39
	v_lshlrev_b32_e32 v68, 16, v42
	v_and_b32_e32 v69, 0xffff0000, v42
	v_lshlrev_b32_e32 v42, 16, v43
	v_and_b32_e32 v43, 0xffff0000, v43
	v_pk_mul_f32 v[38:39], v[36:37], v[40:41]
	v_pk_mul_f32 v[36:37], v[60:61], v[62:63]
	v_pk_mul_f32 v[42:43], v[66:67], v[42:43]
	v_pk_mul_f32 v[40:41], v[64:65], v[68:69]
	v_lshlrev_b32_e32 v70, 16, v48
	v_and_b32_e32 v71, 0xffff0000, v48
	v_lshlrev_b32_e32 v48, 16, v49
	v_and_b32_e32 v49, 0xffff0000, v49
	v_lshlrev_b32_e32 v72, 16, v50
	v_and_b32_e32 v73, 0xffff0000, v50
	v_lshlrev_b32_e32 v50, 16, v51
	v_and_b32_e32 v51, 0xffff0000, v51
	v_pk_fma_f32 v[52:53], v[24:25], v[36:37], v[52:53]
	v_pk_fma_f32 v[54:55], v[26:27], v[38:39], v[54:55]
	v_pk_fma_f32 v[56:57], v[20:21], v[40:41], v[56:57]
	v_pk_fma_f32 v[58:59], v[22:23], v[42:43], v[58:59]
	v_pk_mul_f32 v[48:49], v[54:55], v[48:49]
	v_pk_mul_f32 v[52:53], v[52:53], v[70:71]
	v_pk_mul_f32 v[50:51], v[58:59], v[50:51]
	v_pk_mul_f32 v[54:55], v[56:57], v[72:73]
	v_bfe_u32 v1, v52, 16, 1
	v_bfe_u32 v56, v48, 16, 1
	v_bfe_u32 v58, v54, 16, 1
	v_bfe_u32 v60, v50, 16, 1
	v_bfe_u32 v45, v53, 16, 1
	v_bfe_u32 v57, v49, 16, 1
	v_bfe_u32 v59, v55, 16, 1
	v_bfe_u32 v61, v51, 16, 1
	v_add3_u32 v1, v52, v1, s28
	v_add3_u32 v48, v48, v56, s28
	v_add3_u32 v52, v54, v58, s28
	v_add3_u32 v50, v50, v60, s28
	v_add3_u32 v45, v53, v45, s28
	v_add3_u32 v49, v49, v57, s28
	v_add3_u32 v53, v55, v59, s28
	v_add3_u32 v51, v51, v61, s28
	v_lshrrev_b32_e32 v1, 16, v1
	v_lshrrev_b32_e32 v54, 16, v48
	v_lshrrev_b32_e32 v52, 16, v52
	v_lshrrev_b32_e32 v55, 16, v50
	v_and_or_b32 v48, v45, s25, v1
	v_and_or_b32 v49, v49, s25, v54
	v_and_or_b32 v50, v53, s25, v52
	v_and_or_b32 v51, v51, s25, v55
	global_store_dwordx4 v[2:3], v[48:51], off
	s_cbranch_scc0 .LBB0_715
	s_add_i32 s17, s17, s18
	s_add_i32 s20, s20, s21
	s_add_i32 s22, s22, s23
	s_cmpk_gt_i32 s17, 0x7ff
	s_cbranch_scc0 .LBB0_712
